# out-projection phase: each wave touches its 32 rows of the workgroup's x tile (one dword per 128-byte line) before the prologue stage loads, so the epilogue's residual reads find the tile in the memor
# baseline (speedup 1.0000x reference)
.LBB0_553:
	s_or_b64 exec, exec, s[0:1]
	s_mov_b64 s[6:7], s[46:47]
	v_mov_b32_e32 v8, v186
	s_waitcnt lgkmcnt(0)
	s_barrier
	s_and_b64 vcc, exec, s[24:25]
	v_readfirstlane_b32 s11, v8
	s_cbranch_vccz .LBB0_573
	v_lshlrev_b32_e32 v0, 4, v8
	v_add_u32_e32 v1, 0x2000, v0
	v_ashrrev_i32_e32 v2, 31, v1
	v_lshrrev_b32_e32 v2, 22, v2
	v_add_u32_e32 v2, v1, v2
	v_ashrrev_i32_e32 v9, 10, v2
	v_mul_i32_i24_e32 v3, 0x400, v9
	v_sub_u32_e32 v1, v1, v3
	v_lshrrev_b32_e32 v3, 4, v1
	v_bitop3_b32 v1, v3, v1, 32 bitop3:0x6c
	v_ashrrev_i32_e32 v3, 31, v1
	v_lshrrev_b32_e32 v3, 26, v3
	v_add_u32_e32 v3, v1, v3
	v_ashrrev_i32_e32 v10, 6, v3
	v_and_b32_e32 v3, 0xc0, v3
	v_sub_u32_e32 v1, v1, v3
	v_mov_b32_e32 v3, 1
	v_lshlrev_b32_e32 v2, 5, v9
	v_ashrrev_i16_sdwa v1, v3, sext(v1) dst_sel:DWORD dst_unused:UNUSED_PAD src0_sel:DWORD src1_sel:BYTE_0
	v_and_b32_e32 v2, 32, v2
	v_bfe_i32 v11, v1, 0, 16
	v_add_lshl_u32 v1, v2, v11, 1
	v_lshlrev_b32_e32 v2, 3, v9
	v_and_b32_e32 v2, -16, v2
	s_load_dwordx2 s[0:1], s[6:7], 0x98
	s_load_dwordx2 s[2:3], s[6:7], 0x0
	v_add_u32_e32 v2, v10, v2
	v_and_b32_e32 v4, 3, v10
	s_mov_b32 s6, 0x1fffe0
	v_lshl_add_u32 v136, v2, 11, v1
	v_and_or_b32 v4, v2, s6, v4
	v_lshrrev_b32_e32 v5, 2, v2
	v_lshlrev_b32_e32 v2, 1, v2
	v_and_b32_e32 v5, 4, v5
	v_and_b32_e32 v2, 24, v2
	v_or3_b32 v2, v4, v5, v2
	v_lshl_add_u32 v140, v2, 11, v1
	v_bfe_i32 v2, v8, 27, 1
	v_lshrrev_b32_e32 v2, 22, v2
	v_add_u32_e32 v2, v0, v2
	v_and_b32_e32 v2, 0xfffffc00, v2
	v_sub_u32_e32 v0, v0, v2
	v_lshrrev_b32_e32 v2, 4, v0
	v_bitop3_b32 v2, v2, v0, 32 bitop3:0x6c
	v_ashrrev_i32_e32 v0, 31, v0
	v_lshrrev_b32_e32 v0, 26, v0
	v_ashrrev_i32_e32 v1, 31, v8
	v_add_u32_e32 v0, v2, v0
	v_lshrrev_b32_e32 v1, 26, v1
	v_ashrrev_i32_e32 v13, 6, v0
	v_add_u32_e32 v1, v8, v1
	v_mul_i32_i24_e32 v0, 64, v13
	v_ashrrev_i32_e32 v12, 6, v1
	v_sub_u32_e32 v0, v2, v0
	s_waitcnt lgkmcnt(0)
	s_add_u32 s33, s0, 0x1971b000
	v_lshlrev_b32_e32 v1, 5, v12
	v_ashrrev_i16_sdwa v0, v3, sext(v0) dst_sel:DWORD dst_unused:UNUSED_PAD src0_sel:DWORD src1_sel:BYTE_0
	s_addc_u32 s42, s1, 0
	v_and_b32_e32 v1, 32, v1
	v_bfe_i32 v14, v0, 0, 16
	s_add_u32 s43, s0, 0x87b000
	v_add_lshl_u32 v0, v1, v14, 1
	v_lshlrev_b32_e32 v1, 3, v12
	s_addc_u32 s44, s1, 0
	s_ashr_i32 s8, s11, 6
	v_and_b32_e32 v1, -16, v1
	s_ashr_i32 s12, s11, 8
	s_lshl_b32 s45, s8, 10
	v_add_u32_e32 v1, v13, v1
	v_and_b32_e32 v2, 3, v13
	s_lshl_b32 s7, s63, 5
	v_and_or_b32 v2, v1, s6, v2
	s_mul_i32 s6, s63, 33
	s_and_b64 s[4:5], s[4:5], exec
	s_cselect_b32 s4, s6, s7
	s_add_i32 s4, s4, s62
	s_ashr_i32 s5, s4, 31
	s_lshr_b32 s5, s5, 27
	s_add_i32 s5, s4, s5
	s_ashr_i32 s6, s5, 5
	s_and_b32 s5, s5, 0xffe0
	s_sub_i32 s4, s4, s5
	s_bfe_i32 s5, s4, 0x80000
	s_bfe_u32 s5, s5, 0x3000c
	s_add_i32 s5, s4, s5
	s_bfe_i32 s7, s5, 0x80000
	s_and_b32 s5, s5, 0xf8
	s_sub_i32 s4, s4, s5
	s_lshl_b32 s6, s6, 3
	s_sext_i32_i16 s7, s7
	s_sext_i32_i8 s4, s4
	s_lshr_b32 s10, s7, 3
	s_add_i32 s34, s6, s4
	s_ashr_i32 s35, s34, 31
	s_bfe_i64 s[6:7], s[10:11], 0x100000
	v_lshl_add_u32 v142, v1, 11, v0
	v_lshrrev_b32_e32 v3, 2, v1
	v_lshlrev_b32_e32 v1, 1, v1
	s_lshl_b64 s[4:5], s[34:35], 19
	s_lshl_b64 s[6:7], s[6:7], 19
	v_and_b32_e32 v3, 4, v3
	v_and_b32_e32 v1, 24, v1
	s_add_u32 s38, s43, s6
	v_or3_b32 v1, v2, v3, v1
	s_addc_u32 s39, s44, s7
	s_lshl_b32 s99, s34, 20
	s_add_u32 s100, s2, s99
	s_addc_u32 s101, s3, 0
	s_lshl_b32 s99, s10, 10
	s_add_u32 s100, s100, s99
	s_addc_u32 s101, s101, 0
	v_lshrrev_b32_e32 v236, 6, v186
	v_lshlrev_b32_e32 v236, 5, v236
	v_bfe_u32 v237, v186, 3, 3
	v_add_u32_e32 v236, v236, v237
	v_lshlrev_b32_e32 v236, 12, v236
	v_and_b32_e32 v237, 7, v186
	v_lshl_add_u32 v236, v237, 7, v236
	global_load_dword v238, v236, s[100:101]
	v_add_u32_e32 v236, 0x8000, v236
	global_load_dword v238, v236, s[100:101]
	v_add_u32_e32 v236, 0x8000, v236
	global_load_dword v238, v236, s[100:101]
	v_add_u32_e32 v236, 0x8000, v236
	global_load_dword v238, v236, s[100:101]
	s_add_i32 s46, s45, 0
	v_lshl_add_u32 v146, v1, 11, v0
	s_add_i32 m0, s46, 0x10000
	v_add_u32_e32 v144, 0x40000, v142
	global_load_lds_dwordx4 v146, s[38:39]
	s_add_i32 m0, s46, 0x12000
	s_add_u32 s6, s38, 0x40000
	global_load_lds_dwordx4 v140, s[38:39]
	s_addc_u32 s7, s39, 0
	s_add_i32 m0, s46, 0x14000
	v_add_u32_e32 v138, 0x40000, v136
	global_load_lds_dwordx4 v146, s[6:7]
	s_add_i32 m0, s46, 0x16000
	s_add_u32 s36, s33, s4
	global_load_lds_dwordx4 v140, s[6:7]
	s_addc_u32 s37, s42, s5
	s_mov_b32 m0, s46
	s_add_i32 s47, s46, 0x2000
	global_load_lds_dwordx4 v142, s[36:37]
	s_mov_b32 m0, s47
	s_add_i32 s48, s46, 0x4000
	global_load_lds_dwordx4 v136, s[36:37]
	s_mov_b32 m0, s48
	s_add_i32 s49, s46, 0x6000
	global_load_lds_dwordx4 v144, s[36:37]
	s_mov_b32 m0, s49
	v_mov_b32_e32 v147, 0
	global_load_lds_dwordx4 v138, s[36:37]
	v_mov_b32_e32 v141, v147
	v_mov_b32_e32 v143, v147
	v_mov_b32_e32 v137, v147
	s_cmp_eq_u32 s12, 1
	s_mov_b32 s13, 0x40000
	s_mov_b32 s50, 0
	v_lshl_add_u64 v[6:7], s[38:39], 0, v[146:147]
	v_lshl_add_u64 v[4:5], s[38:39], 0, v[140:141]
	v_lshl_add_u64 v[0:1], s[36:37], 0, v[142:143]
	s_cselect_b64 s[4:5], -1, 0
	s_cmp_lg_u32 s12, 1
	v_lshl_add_u64 v[2:3], s[36:37], 0, v[136:137]
	s_cbranch_scc1 .LBB0_556
	s_barrier
